# baseline (speedup 1.0000x reference)
.LBB3_8:
	s_or_b64 exec, exec, s[6:7]
	s_lshl_b32 s3, s2, 2
	s_and_b32 s26, s3, 28
	s_lshr_b32 s3, s2, 6
	s_lshl_b32 s2, s2, 1
	s_add_i32 s26, s26, s3
	s_and_b32 s22, s2, 64
	v_lshrrev_b32_e32 v47, 3, v0
	s_movk_i32 s2, 0x20f
	s_lshl_b32 s23, s26, 2
	v_mov_b32_e32 v4, 0xffffffbe
	v_cmp_lt_u32_e64 s[6:7], s2, v0
	v_or_b32_e32 v66, 64, v47
	v_mul_lo_u16_e32 v6, 63, v66
	v_cndmask_b32_e64 v70, 0, v4, s[6:7]
	v_mov_b32_e32 v4, s23
	s_add_i32 s25, s23, -1
	s_add_i32 s27, s22, -1
	v_lshlrev_b32_e32 v28, 3, v0
	v_addc_co_u32_e64 v71, vcc, -1, v4, s[6:7]
	v_mov_b32_e32 v8, 0x7f
	v_lshrrev_b16_e32 v65, 12, v6
	v_and_b32_e32 v30, 56, v28
	v_med3_i32 v4, v71, 0, v8
	v_add3_u32 v5, s27, v47, v70
	v_mul_i32_i24_e32 v68, 0xffffffbe, v65
	v_add_u32_e32 v67, s25, v65
	v_lshlrev_b32_e32 v26, 1, v30
	v_mov_b32_e32 v27, 0
	v_med3_i32 v5, v5, 0, v8
	v_lshlrev_b32_e32 v4, 14, v4
	v_med3_i32 v6, v67, 0, v8
	v_add3_u32 v7, s27, v66, v68
	s_waitcnt lgkmcnt(0)
	v_lshl_add_u64 v[2:3], s[12:13], 0, v[26:27]
	v_lshl_or_b32 v26, v5, 7, v4
	v_med3_i32 v7, v7, 0, v8
	v_lshlrev_b32_e32 v6, 14, v6
	v_lshl_add_u64 v[4:5], v[2:3], 0, v[26:27]
	v_lshl_or_b32 v26, v7, 7, v6
	v_or_b32_e32 v62, 0x80, v47
	v_lshl_add_u64 v[6:7], v[2:3], 0, v[26:27]
	global_load_dwordx4 v[42:45], v[4:5], off
	global_load_dwordx4 v[22:25], v[6:7], off
	v_mul_lo_u16_e32 v4, 0xf9, v62
	v_or_b32_e32 v58, 0xc0, v47
	v_lshrrev_b16_e32 v61, 14, v4
	v_mul_u32_u24_e32 v6, 0x3e1, v58
	v_mul_i32_i24_e32 v64, 0xffffffbe, v61
	v_add_u32_e32 v63, s25, v61
	v_lshrrev_b32_e32 v57, 16, v6
	v_min_u32_e32 v4, 0x7f, v63
	v_add3_u32 v5, s27, v62, v64
	v_mul_i32_i24_e32 v60, 0xffffffbe, v57
	v_add_u32_e32 v59, s25, v57
	v_med3_i32 v5, v5, 0, v8
	v_lshlrev_b32_e32 v4, 14, v4
	v_min_u32_e32 v6, 0x7f, v59
	v_add3_u32 v7, s27, v58, v60
	v_lshl_or_b32 v26, v5, 7, v4
	v_med3_i32 v7, v7, 0, v8
	v_lshlrev_b32_e32 v6, 14, v6
	v_lshl_add_u64 v[4:5], v[2:3], 0, v[26:27]
	v_lshl_or_b32 v26, v7, 7, v6
	v_or_b32_e32 v54, 0x100, v47
	v_lshl_add_u64 v[6:7], v[2:3], 0, v[26:27]
	global_load_dwordx4 v[18:21], v[4:5], off
	global_load_dwordx4 v[14:17], v[6:7], off
	v_mul_u32_u24_e32 v4, 0x3e1, v54
	v_lshrrev_b32_e32 v53, 16, v4
	v_or_b32_e32 v52, 0x140, v47
	s_movk_i32 s3, 0xffbe
	v_mul_i32_i24_e32 v56, 0xffffffbe, v53
	v_add_u32_e32 v55, s25, v53
	v_mul_u32_u24_e32 v6, 0x3e1, v52
	v_min_u32_e32 v4, 0x7f, v55
	v_add3_u32 v5, s27, v54, v56
	v_mul_i32_i24_sdwa v7, v6, s3 dst_sel:DWORD dst_unused:UNUSED_PAD src0_sel:WORD_1 src1_sel:DWORD
	v_add_u32_sdwa v6, s25, v6 dst_sel:DWORD dst_unused:UNUSED_PAD src0_sel:DWORD src1_sel:WORD_1
	v_med3_i32 v5, v5, 0, v8
	v_lshlrev_b32_e32 v4, 14, v4
	v_min_u32_e32 v6, 0x7f, v6
	v_add3_u32 v7, s27, v52, v7
	v_lshl_or_b32 v26, v5, 7, v4
	v_med3_i32 v7, v7, 0, v8
	v_lshlrev_b32_e32 v6, 14, v6
	v_lshl_add_u64 v[4:5], v[2:3], 0, v[26:27]
	v_lshl_or_b32 v26, v7, 7, v6
	v_or_b32_e32 v51, 0x180, v47
	v_lshl_add_u64 v[32:33], v[2:3], 0, v[26:27]
	global_load_dwordx4 v[10:13], v[4:5], off
	global_load_dwordx4 v[6:9], v[32:33], off
	v_min_u32_e32 v4, 0x18b, v51
	s_min_u32 s2, s23, 0x7b
	v_add_u32_e32 v4, s27, v4
	v_add_u32_e32 v4, 0xfffffeb6, v4
	s_lshl_b32 s2, s2, 14
	v_min_u32_e32 v4, 0x7f, v4
	s_add_i32 s2, s2, 0x10000
	v_lshl_or_b32 v26, v4, 7, s2
	v_lshl_add_u64 v[2:3], v[2:3], 0, v[26:27]
	global_load_dwordx4 v[2:5], v[2:3], off
	s_load_dwordx4 s[16:19], s[0:1], 0x10
	v_and_b32_e32 v28, 63, v0
	v_lshlrev_b32_e32 v28, 3, v28
	global_load_dwordx2 v[26:27], v28, s[14:15]
	global_load_dwordx2 v[172:173], v28, s[14:15] offset:512
	global_load_dwordx2 v[174:175], v28, s[14:15] offset:1024
	global_load_dwordx2 v[176:177], v28, s[14:15] offset:1536
	v_lshlrev_b32_e32 v28, 2, v1
	s_waitcnt lgkmcnt(0)
	global_load_dword v32, v28, s[16:17]
	global_load_dword v31, v28, s[18:19]
	s_movk_i32 s38, 0xff94
	s_movk_i32 s39, 0xffee
	s_add_i32 s40, s22, -4
	v_mov_b32_e32 v131, 0x7f
	v_mov_b32_e32 v132, 0x7c
	v_min_u32_e32 v133, 27, v50
	v_min_u32_e32 v134, 3, v48
	v_or_b32_e32 v134, 24, v134
	v_lshl_or_b32 v128, v48, 6, v1
	v_mul_u32_u24_e32 v129, 0x25f, v128
	v_lshrrev_b32_e32 v129, 16, v129
	v_mad_i32_i24 v128, v129, s38, v128
	v_mul_u32_u24_e32 v130, 0xe39, v128
	v_lshrrev_b32_e32 v130, 16, v130
	v_mad_i32_i24 v128, v130, s39, v128
	v_add_u32_e32 v130, s25, v130
	v_med3_i32 v130, v130, 0, v131
	v_lshl_add_u32 v128, v128, 2, s40
	v_med3_i32 v128, v128, 0, v132
	v_min_u32_e32 v129, 15, v129
	v_lshlrev_b32_e32 v129, 14, v129
	v_lshlrev_b32_e32 v130, 7, v130
	v_or3_b32 v94, v130, v129, v128
	v_lshl_or_b32 v128, v49, 6, v1
	v_mul_u32_u24_e32 v129, 0x25f, v128
	v_lshrrev_b32_e32 v129, 16, v129
	v_mad_i32_i24 v128, v129, s38, v128
	v_mul_u32_u24_e32 v130, 0xe39, v128
	v_lshrrev_b32_e32 v130, 16, v130
	v_mad_i32_i24 v128, v130, s39, v128
	v_add_u32_e32 v130, s25, v130
	v_med3_i32 v130, v130, 0, v131
	v_lshl_add_u32 v128, v128, 2, s40
	v_med3_i32 v128, v128, 0, v132
	v_min_u32_e32 v129, 15, v129
	v_lshlrev_b32_e32 v129, 14, v129
	v_lshlrev_b32_e32 v130, 7, v130
	v_or3_b32 v96, v130, v129, v128
	v_lshl_or_b32 v128, v133, 6, v1
	v_mul_u32_u24_e32 v129, 0x25f, v128
	v_lshrrev_b32_e32 v129, 16, v129
	v_mad_i32_i24 v128, v129, s38, v128
	v_mul_u32_u24_e32 v130, 0xe39, v128
	v_lshrrev_b32_e32 v130, 16, v130
	v_mad_i32_i24 v128, v130, s39, v128
	v_add_u32_e32 v130, s25, v130
	v_med3_i32 v130, v130, 0, v131
	v_lshl_add_u32 v128, v128, 2, s40
	v_med3_i32 v128, v128, 0, v132
	v_min_u32_e32 v129, 15, v129
	v_lshlrev_b32_e32 v129, 14, v129
	v_lshlrev_b32_e32 v130, 7, v130
	v_or3_b32 v98, v130, v129, v128
	v_lshl_or_b32 v128, v134, 6, v1
	v_mul_u32_u24_e32 v129, 0x25f, v128
	v_lshrrev_b32_e32 v129, 16, v129
	v_mad_i32_i24 v128, v129, s38, v128
	v_mul_u32_u24_e32 v130, 0xe39, v128
	v_lshrrev_b32_e32 v130, 16, v130
	v_mad_i32_i24 v128, v130, s39, v128
	v_add_u32_e32 v130, s25, v130
	v_med3_i32 v130, v130, 0, v131
	v_lshl_add_u32 v128, v128, 2, s40
	v_med3_i32 v128, v128, 0, v132
	v_min_u32_e32 v129, 15, v129
	v_lshlrev_b32_e32 v129, 14, v129
	v_lshlrev_b32_e32 v130, 7, v130
	v_or3_b32 v100, v130, v129, v128
	v_cmp_eq_u32_e32 vcc, 27, v134
	v_readfirstlane_b32 s41, v100
	s_nop 1
	v_mov_b32_e32 v135, s41
	v_cndmask_b32_e32 v100, v100, v135, vcc
	v_accvgpr_write_b32 a3, 0
	v_accvgpr_write_b32 a2, 0
	v_accvgpr_write_b32 a1, 0
	v_accvgpr_write_b32 a0, 0
	v_accvgpr_write_b32 a7, 0
	v_accvgpr_write_b32 a6, 0
	v_accvgpr_write_b32 a5, 0
	v_accvgpr_write_b32 a4, 0
	v_accvgpr_write_b32 a15, 0
	v_accvgpr_write_b32 a14, 0
	v_accvgpr_write_b32 a13, 0
	v_accvgpr_write_b32 a12, 0
	v_accvgpr_write_b32 a19, 0
	v_accvgpr_write_b32 a18, 0
	v_accvgpr_write_b32 a17, 0
	v_accvgpr_write_b32 a16, 0
	v_accvgpr_write_b32 a31, 0
	v_accvgpr_write_b32 a30, 0
	v_accvgpr_write_b32 a29, 0
	v_accvgpr_write_b32 a28, 0
	v_accvgpr_write_b32 a63, 0
	v_accvgpr_write_b32 a62, 0
	v_accvgpr_write_b32 a61, 0
	v_accvgpr_write_b32 a60, 0
	v_accvgpr_write_b32 a11, 0
	v_accvgpr_write_b32 a10, 0
	v_accvgpr_write_b32 a9, 0
	v_accvgpr_write_b32 a8, 0
	v_accvgpr_write_b32 a23, 0
	v_accvgpr_write_b32 a22, 0
	v_accvgpr_write_b32 a21, 0
	v_accvgpr_write_b32 a20, 0
	v_accvgpr_write_b32 a27, 0
	v_accvgpr_write_b32 a26, 0
	v_accvgpr_write_b32 a25, 0
	v_accvgpr_write_b32 a24, 0
	v_accvgpr_write_b32 a39, 0
	v_accvgpr_write_b32 a38, 0
	v_accvgpr_write_b32 a37, 0
	v_accvgpr_write_b32 a36, 0
	v_accvgpr_write_b32 a47, 0
	v_accvgpr_write_b32 a46, 0
	v_accvgpr_write_b32 a45, 0
	v_accvgpr_write_b32 a44, 0
	v_accvgpr_write_b32 a67, 0
	v_accvgpr_write_b32 a66, 0
	v_accvgpr_write_b32 a65, 0
	v_accvgpr_write_b32 a64, 0
	v_accvgpr_write_b32 a35, 0
	v_accvgpr_write_b32 a34, 0
	v_accvgpr_write_b32 a33, 0
	v_accvgpr_write_b32 a32, 0
	v_accvgpr_write_b32 a43, 0
	v_accvgpr_write_b32 a42, 0
	v_accvgpr_write_b32 a41, 0
	v_accvgpr_write_b32 a40, 0
	v_accvgpr_write_b32 a51, 0
	v_accvgpr_write_b32 a50, 0
	v_accvgpr_write_b32 a49, 0
	v_accvgpr_write_b32 a48, 0
	v_accvgpr_write_b32 a55, 0
	v_accvgpr_write_b32 a54, 0
	v_accvgpr_write_b32 a53, 0
	v_accvgpr_write_b32 a52, 0
	v_accvgpr_write_b32 a59, 0
	v_accvgpr_write_b32 a58, 0
	v_accvgpr_write_b32 a57, 0
	v_accvgpr_write_b32 a56, 0
	v_accvgpr_write_b32 a71, 0
	v_accvgpr_write_b32 a70, 0
	v_accvgpr_write_b32 a69, 0
	v_accvgpr_write_b32 a68, 0
	v_readfirstlane_b32 s42, v118
	v_and_b32_e32 v130, 63, v0
	v_lshlrev_b32_e32 v130, 4, v130
	v_bfe_u32 v131, v0, 6, 2
	v_bfe_u32 v132, v0, 4, 2
	v_lshrrev_b32_e32 v133, 8, v0
	v_and_b32_e32 v129, 15, v0
	v_lshl_or_b32 v133, v133, 4, v129
	s_add_i32 s43, s42, 0x2000
	s_add_i32 s44, s42, 0x4000
	v_add_u32_e32 v137, s42, v130
	v_add_u32_e32 v138, 0x2000, v137
	v_add_u32_e32 v139, 0x4000, v137
	v_add_u32_e32 v164, 0xc600, v130
	v_add_u32_e32 v165, 0x10e00, v130
	v_add_u32_e32 v166, 0x16000, v130
	v_add_u32_e32 v167, 0x1a800, v130
	v_add_u32_e32 v168, 0x1f000, v130
	s_add_u32 s52, s50, 0x9000
	s_addc_u32 s53, s51, 0
	s_add_i32 m0, s42, 0x16000
	s_nop 0
	global_load_lds_dwordx4 v137, s[52:53]
	s_add_i32 m0, s43, 0x16000
	s_nop 0
	global_load_lds_dwordx4 v138, s[52:53]
	s_cmp_lt_u32 s42, 0x800
	s_cbranch_scc0 .Lk4_sp2
	s_add_i32 m0, s44, 0x16000
	s_nop 0
	global_load_lds_dwordx4 v139, s[52:53]

.Lk4_sp4:
	v_lshl_add_u32 v128, v131, 1, 0
	v_lshl_add_u32 v128, v128, 5, v128
	v_add3_u32 v128, v128, v133, 0
	v_bitop3_b32 v129, v128, v132, 7 bitop3:0x6c
	v_lshlrev_b32_e32 v128, 7, v128
	v_lshl_or_b32 v140, v129, 4, v128
	v_xor_b32_e32 v141, 64, v140
	v_lshl_add_u32 v128, v131, 1, 1
	v_lshl_add_u32 v128, v128, 5, v128
	v_add3_u32 v128, v128, v133, 0
	v_bitop3_b32 v129, v128, v132, 7 bitop3:0x6c
	v_lshlrev_b32_e32 v128, 7, v128
	v_lshl_or_b32 v142, v129, 4, v128
	v_xor_b32_e32 v143, 64, v142
	v_lshl_add_u32 v128, v131, 1, 0
	v_lshl_add_u32 v128, v128, 5, v128
	v_add3_u32 v128, v128, v133, 1
	v_bitop3_b32 v129, v128, v132, 7 bitop3:0x6c
	v_lshlrev_b32_e32 v128, 7, v128
	v_lshl_or_b32 v144, v129, 4, v128
	v_xor_b32_e32 v145, 64, v144
	v_lshl_add_u32 v128, v131, 1, 1
	v_lshl_add_u32 v128, v128, 5, v128
	v_add3_u32 v128, v128, v133, 1
	v_bitop3_b32 v129, v128, v132, 7 bitop3:0x6c
	v_lshlrev_b32_e32 v128, 7, v128
	v_lshl_or_b32 v146, v129, 4, v128
	v_xor_b32_e32 v147, 64, v146
	v_lshl_add_u32 v128, v131, 1, 2
	v_lshl_add_u32 v128, v128, 5, v128
	v_add3_u32 v128, v128, v133, 0
	v_bitop3_b32 v129, v128, v132, 7 bitop3:0x6c
	v_lshlrev_b32_e32 v128, 7, v128
	v_lshl_or_b32 v148, v129, 4, v128
	v_xor_b32_e32 v149, 64, v148
	v_lshl_add_u32 v128, v131, 1, 3
	v_lshl_add_u32 v128, v128, 5, v128
	v_add3_u32 v128, v128, v133, 0
	v_bitop3_b32 v129, v128, v132, 7 bitop3:0x6c
	v_lshlrev_b32_e32 v128, 7, v128
	v_lshl_or_b32 v150, v129, 4, v128
	v_xor_b32_e32 v151, 64, v150
	v_lshl_add_u32 v128, v131, 1, 2
	v_lshl_add_u32 v128, v128, 5, v128
	v_add3_u32 v128, v128, v133, 1
	v_bitop3_b32 v129, v128, v132, 7 bitop3:0x6c
	v_lshlrev_b32_e32 v128, 7, v128
	v_lshl_or_b32 v152, v129, 4, v128
	v_xor_b32_e32 v153, 64, v152
	v_lshl_add_u32 v128, v131, 1, 3
	v_lshl_add_u32 v128, v128, 5, v128
	v_add3_u32 v128, v128, v133, 1
	v_bitop3_b32 v129, v128, v132, 7 bitop3:0x6c
	v_lshlrev_b32_e32 v128, 7, v128
	v_lshl_or_b32 v154, v129, 4, v128
	v_xor_b32_e32 v155, 64, v154
	v_lshl_add_u32 v128, v131, 1, 4
	v_lshl_add_u32 v128, v128, 5, v128
	v_add3_u32 v128, v128, v133, 0
	v_bitop3_b32 v129, v128, v132, 7 bitop3:0x6c
	v_lshlrev_b32_e32 v128, 7, v128
	v_lshl_or_b32 v156, v129, 4, v128
	v_xor_b32_e32 v157, 64, v156
	v_lshl_add_u32 v128, v131, 1, 5
	v_lshl_add_u32 v128, v128, 5, v128
	v_add3_u32 v128, v128, v133, 0
	v_bitop3_b32 v129, v128, v132, 7 bitop3:0x6c
	v_lshlrev_b32_e32 v128, 7, v128
	v_lshl_or_b32 v158, v129, 4, v128
	v_xor_b32_e32 v159, 64, v158
	v_lshl_add_u32 v128, v131, 1, 4
	v_lshl_add_u32 v128, v128, 5, v128
	v_add3_u32 v128, v128, v133, 1
	v_bitop3_b32 v129, v128, v132, 7 bitop3:0x6c
	v_lshlrev_b32_e32 v128, 7, v128
	v_lshl_or_b32 v160, v129, 4, v128
	v_xor_b32_e32 v161, 64, v160
	v_lshl_add_u32 v128, v131, 1, 5
	v_lshl_add_u32 v128, v128, 5, v128
	v_add3_u32 v128, v128, v133, 1
	v_bitop3_b32 v129, v128, v132, 7 bitop3:0x6c
	v_lshlrev_b32_e32 v128, 7, v128
	v_lshl_or_b32 v162, v129, 4, v128
	v_xor_b32_e32 v163, 64, v162
	s_waitcnt vmcnt(6)
	v_pk_add_f32 v[26:27], v[26:27], v[172:173]
	v_pk_add_f32 v[174:175], v[174:175], v[176:177]
	v_pk_add_f32 v[26:27], v[26:27], v[174:175]
	s_nop 1
	v_mov_b32_dpp v28, v26 row_shr:1 row_mask:0xf bank_mask:0xf bound_ctrl:1
	v_mov_b32_dpp v29, v27 row_shr:1 row_mask:0xf bank_mask:0xf bound_ctrl:1
	v_pk_add_f32 v[26:27], v[26:27], v[28:29]
	v_mov_b32_e32 v34, 0
	v_mov_b32_e32 v35, 0
	v_mov_b32_dpp v28, v26 row_shr:2 row_mask:0xf bank_mask:0xf bound_ctrl:1
	v_mov_b32_dpp v29, v27 row_shr:2 row_mask:0xf bank_mask:0xf bound_ctrl:1
	v_pk_add_f32 v[26:27], v[26:27], v[28:29]
	v_cmp_eq_u32_e32 vcc, 63, v1
	s_nop 0
	v_mov_b32_dpp v28, v26 row_shr:4 row_mask:0xf bank_mask:0xf bound_ctrl:1
	v_mov_b32_dpp v29, v27 row_shr:4 row_mask:0xf bank_mask:0xf bound_ctrl:1
	v_pk_add_f32 v[26:27], v[26:27], v[28:29]
	s_nop 1
	v_mov_b32_dpp v28, v26 row_shr:8 row_mask:0xf bank_mask:0xf bound_ctrl:1
	v_mov_b32_dpp v29, v27 row_shr:8 row_mask:0xf bank_mask:0xf bound_ctrl:1
	v_pk_add_f32 v[28:29], v[26:27], v[28:29]
	v_mov_b32_e32 v27, 0
	v_mov_b32_e32 v26, 0
	v_mov_b32_dpp v34, v28 row_bcast:15 row_mask:0xa bank_mask:0xf
	v_mov_b32_dpp v35, v29 row_bcast:15 row_mask:0xa bank_mask:0xf
	v_pk_add_f32 v[28:29], v[28:29], v[34:35]
	s_nop 1
	v_mov_b32_dpp v26, v28 row_bcast:31 row_mask:0xc bank_mask:0xf
	v_mov_b32_dpp v27, v29 row_bcast:31 row_mask:0xc bank_mask:0xf
	v_pk_add_f32 v[26:27], v[28:29], v[26:27]
	s_nop 1
	v_readlane_b32 s46, v26, 63
	v_readlane_b32 s47, v27, 63
	v_cmp_gt_u32_e32 vcc, 64, v0
	s_mov_b32 s2, 0xf800000
	s_and_saveexec_b64 s[10:11], vcc
	s_cbranch_execz .LBB3_16
	v_mov_b32_e32 v26, s46
	v_mov_b32_e32 v27, s47
	v_mul_f32_e32 v26, 0x35800000, v26
	v_mul_f32_e32 v27, 0x35800000, v27
	v_fma_f32 v27, -v26, v26, v27
	v_add_f32_e32 v27, 0x3727c5ac, v27
	v_mul_f32_e32 v28, 0x4f800000, v27
	v_cmp_gt_f32_e32 vcc, s2, v27
	s_nop 1
	v_cndmask_b32_e32 v27, v27, v28, vcc
	v_sqrt_f32_e32 v28, v27
	s_nop 0
	v_add_u32_e32 v29, -1, v28
	v_fma_f32 v33, -v29, v28, v27
	v_cmp_ge_f32_e64 s[2:3], 0, v33
	v_add_u32_e32 v33, 1, v28
	s_nop 0
	v_cndmask_b32_e64 v29, v28, v29, s[2:3]
	v_fma_f32 v28, -v33, v28, v27
	v_cmp_lt_f32_e64 s[2:3], 0, v28
	s_nop 1
	v_cndmask_b32_e64 v28, v29, v33, s[2:3]
	v_mul_f32_e32 v29, 0x37800000, v28
	v_cndmask_b32_e32 v28, v28, v29, vcc
	v_mov_b32_e32 v29, 0x260
	v_cmp_class_f32_e32 vcc, v27, v29
	s_nop 1
	v_cndmask_b32_e32 v27, v28, v27, vcc
	v_div_scale_f32 v28, s[2:3], v27, v27, 1.0
	v_rcp_f32_e32 v29, v28
	s_nop 0
	v_fma_f32 v33, -v28, v29, 1.0
	v_fmac_f32_e32 v29, v33, v29
	v_div_scale_f32 v33, vcc, 1.0, v27, 1.0
	v_mul_f32_e32 v34, v33, v29
	v_fma_f32 v35, -v28, v34, v33
	v_fmac_f32_e32 v34, v35, v29
	v_fma_f32 v28, -v28, v34, v33
	v_div_fmas_f32 v28, v28, v29, v34
	v_div_fixup_f32 v27, v28, v27, 1.0
	v_lshl_add_u32 v28, v0, 2, 0
	v_mul_f32_e32 v27, v32, v27
	v_add_u32_e32 v29, 0x15600, v28
	ds_write_b32 v29, v27
	v_fma_f32 v26, -v26, v27, v31
	v_add_u32_e32 v27, 0x15700, v28
	ds_write_b32 v27, v26

	.amdhsa_kernel _Z7kfinal3PKDF16_PKfS2_S2_PK15HIP_vector_typeIjLj4EES2_Pf
		.amdhsa_group_segment_fixed_size 0
		.amdhsa_private_segment_fixed_size 0
		.amdhsa_kernarg_size 56
		.amdhsa_user_sgpr_count 2
		.amdhsa_user_sgpr_dispatch_ptr 0
		.amdhsa_user_sgpr_queue_ptr 0
		.amdhsa_user_sgpr_kernarg_segment_ptr 1
		.amdhsa_user_sgpr_dispatch_id 0
		.amdhsa_user_sgpr_kernarg_preload_length 0
		.amdhsa_user_sgpr_kernarg_preload_offset 0
		.amdhsa_user_sgpr_private_segment_size 0
		.amdhsa_uses_dynamic_stack 0
		.amdhsa_enable_private_segment 0
		.amdhsa_system_sgpr_workgroup_id_x 1
		.amdhsa_system_sgpr_workgroup_id_y 0
		.amdhsa_system_sgpr_workgroup_id_z 0
		.amdhsa_system_sgpr_workgroup_info 0
		.amdhsa_system_vgpr_workitem_id 0
		.amdhsa_next_free_vgpr 253
		.amdhsa_next_free_sgpr 54
		.amdhsa_accum_offset 180
		.amdhsa_reserve_vcc 1
		.amdhsa_float_round_mode_32 0
		.amdhsa_float_round_mode_16_64 0
		.amdhsa_float_denorm_mode_32 3
		.amdhsa_float_denorm_mode_16_64 3
		.amdhsa_dx10_clamp 1
		.amdhsa_ieee_mode 1
		.amdhsa_fp16_overflow 0
		.amdhsa_tg_split 0
		.amdhsa_exception_fp_ieee_invalid_op 0
		.amdhsa_exception_fp_denorm_src 0
		.amdhsa_exception_fp_ieee_div_zero 0
		.amdhsa_exception_fp_ieee_overflow 0
		.amdhsa_exception_fp_ieee_underflow 0
		.amdhsa_exception_fp_ieee_inexact 0
		.amdhsa_exception_int_div_zero 0
	.end_amdhsa_kernel

amdhsa.kernels:
  - .agpr_count:     0
    .args:
      - .actual_access:  read_only
        .address_space:  global
        .offset:         0
        .size:           8
        .value_kind:     global_buffer
      - .actual_access:  read_only
        .address_space:  global
        .offset:         8
        .size:           8
        .value_kind:     global_buffer
      - .actual_access:  read_only
        .address_space:  global
        .offset:         16
        .size:           8
        .value_kind:     global_buffer
      - .actual_access:  read_only
        .address_space:  global
        .offset:         24
        .size:           8
        .value_kind:     global_buffer
      - .actual_access:  read_only
        .address_space:  global
        .offset:         32
        .size:           8
        .value_kind:     global_buffer
      - .actual_access:  read_only
        .address_space:  global
        .offset:         40
        .size:           8
        .value_kind:     global_buffer
      - .actual_access:  write_only
        .address_space:  global
        .offset:         48
        .size:           8
        .value_kind:     global_buffer
      - .actual_access:  write_only
        .address_space:  global
        .offset:         56
        .size:           8
        .value_kind:     global_buffer
      - .actual_access:  write_only
        .address_space:  global
        .offset:         64
        .size:           8
        .value_kind:     global_buffer
      - .actual_access:  write_only
        .address_space:  global
        .offset:         72
        .size:           8
        .value_kind:     global_buffer
    .group_segment_fixed_size: 12000
    .kernarg_segment_align: 8
    .kernarg_segment_size: 80
    .language:       OpenCL C
    .language_version:
      - 2
      - 0
    .max_flat_workgroup_size: 256
    .name:           _Z2k0PKfS0_S0_S0_S0_S0_PDF16_PfS1_S1_
    .private_segment_fixed_size: 0
    .sgpr_count:     24
    .sgpr_spill_count: 0
    .symbol:         _Z2k0PKfS0_S0_S0_S0_S0_PDF16_PfS1_S1_.kd
    .uniform_work_group_size: 1
    .uses_dynamic_stack: false
    .vgpr_count:     150
    .vgpr_spill_count: 0
    .wavefront_size: 64
  - .agpr_count:     16
    .args:
      - .actual_access:  read_only
        .address_space:  global
        .offset:         0
        .size:           8
        .value_kind:     global_buffer
      - .actual_access:  read_only
        .address_space:  global
        .offset:         8
        .size:           8
        .value_kind:     global_buffer
      - .actual_access:  read_only
        .address_space:  global
        .offset:         16
        .size:           8
        .value_kind:     global_buffer
      - .actual_access:  read_only
        .address_space:  global
        .offset:         24
        .size:           8
        .value_kind:     global_buffer
      - .actual_access:  read_only
        .address_space:  global
        .offset:         32
        .size:           8
        .value_kind:     global_buffer
      - .actual_access:  write_only
        .address_space:  global
        .offset:         40
        .size:           8
        .value_kind:     global_buffer
      - .actual_access:  write_only
        .address_space:  global
        .offset:         48
        .size:           8
        .value_kind:     global_buffer
    .group_segment_fixed_size: 14112
    .kernarg_segment_align: 8
    .kernarg_segment_size: 56
    .language:       OpenCL C
    .language_version:
      - 2
      - 0
    .max_flat_workgroup_size: 256
    .name:           _Z4khidPKDF16_PKfS2_S2_S0_PDF16_Pf
    .private_segment_fixed_size: 0
    .sgpr_count:     26
    .sgpr_spill_count: 0
    .symbol:         _Z4khidPKDF16_PKfS2_S2_S0_PDF16_Pf.kd
    .uniform_work_group_size: 1
    .uses_dynamic_stack: false
    .vgpr_count:     156
    .vgpr_spill_count: 0
    .wavefront_size: 64
  - .agpr_count:     144
    .args:
      - .actual_access:  read_only
        .address_space:  global
        .offset:         0
        .size:           8
        .value_kind:     global_buffer
      - .actual_access:  read_only
        .address_space:  global
        .offset:         8
        .size:           8
        .value_kind:     global_buffer
      - .actual_access:  read_only
        .address_space:  global
        .offset:         16
        .size:           8
        .value_kind:     global_buffer
      - .actual_access:  read_only
        .address_space:  global
        .offset:         24
        .size:           8
        .value_kind:     global_buffer
      - .address_space:  global
        .offset:         32
        .size:           8
        .value_kind:     global_buffer
      - .address_space:  global
        .offset:         40
        .size:           8
        .value_kind:     global_buffer
      - .address_space:  global
        .offset:         48
        .size:           8
        .value_kind:     global_buffer
    .group_segment_fixed_size: 0
    .kernarg_segment_align: 8
    .kernarg_segment_size: 56
    .language:       OpenCL C
    .language_version:
      - 2
      - 0
    .max_flat_workgroup_size: 256
    .name:           _Z6kfinalPKDF16_PKfS2_S2_PK15HIP_vector_typeIjLj4EES2_Pf
    .private_segment_fixed_size: 0
    .sgpr_count:     41
    .sgpr_spill_count: 0
    .symbol:         _Z6kfinalPKDF16_PKfS2_S2_PK15HIP_vector_typeIjLj4EES2_Pf.kd
    .uniform_work_group_size: 1
    .uses_dynamic_stack: false
    .vgpr_count:     400
    .vgpr_spill_count: 0
    .wavefront_size: 64
  - .agpr_count:     73
    .args:
      - .actual_access:  read_only
        .address_space:  global
        .offset:         0
        .size:           8
        .value_kind:     global_buffer
      - .actual_access:  read_only
        .address_space:  global
        .offset:         8
        .size:           8
        .value_kind:     global_buffer
      - .actual_access:  read_only
        .address_space:  global
        .offset:         16
        .size:           8
        .value_kind:     global_buffer
      - .actual_access:  read_only
        .address_space:  global
        .offset:         24
        .size:           8
        .value_kind:     global_buffer
      - .address_space:  global
        .offset:         32
        .size:           8
        .value_kind:     global_buffer
      - .address_space:  global
        .offset:         40
        .size:           8
        .value_kind:     global_buffer
      - .address_space:  global
        .offset:         48
        .size:           8
        .value_kind:     global_buffer
    .group_segment_fixed_size: 0
    .kernarg_segment_align: 8
    .kernarg_segment_size: 56
    .language:       OpenCL C
    .language_version:
      - 2
      - 0
    .max_flat_workgroup_size: 512
    .name:           _Z7kfinal3PKDF16_PKfS2_S2_PK15HIP_vector_typeIjLj4EES2_Pf
    .private_segment_fixed_size: 0
    .sgpr_count:     60
    .sgpr_spill_count: 0
    .symbol:         _Z7kfinal3PKDF16_PKfS2_S2_PK15HIP_vector_typeIjLj4EES2_Pf.kd
    .uniform_work_group_size: 1
    .uses_dynamic_stack: false
    .vgpr_count:     253
    .vgpr_spill_count: 0
    .wavefront_size: 64
